# v50 with the out-projection epilogue's stores marked nt (streaming)
# baseline (speedup 1.0000x reference)
; __device__ __forceinline__ unsigned cvt_pk_bf16(float lo, float hi) { unsigned r; asm volatile("v_cvt_pk_bf16_f32 %0, %1, %2" : "=v"(r) : "v"(lo), "v"(hi)); return r; }
;     __device__ __forceinline__ void operator()(const f32x4 (&acc)[2][2][4][2], const pg8::Unit& u, int wr, int wc, int fr, int fq) const {
;         const int row0 = u.pm * 256 + wr * 64 + fr, col0 = u.pn * 256 + wc * 32 + 8 * fq, b = (u.pm * 256) / S;
;         f32x4 gv[2][2];
; #pragma unroll
;         for (int bj = 0; bj < 2; ++bj)
; #pragma unroll
;             for (int n = 0; n < 2; ++n) gv[bj][n] = *(const f32x4*)(gm + (size_t)b * 6144 + col0 + bj * 128 + n * 4);
;     ...
;         constexpr int PF = 4;
;         if (xin32) {
;             f32x4 xq[PF][2];
; #pragma unroll
;             for (int it = 0; it < PF; ++it) { xq[it][0] = __builtin_nontemporal_load((const f32x4*)(xin32 + EO_OFF(it))); xq[it][1] = __builtin_nontemporal_load((const f32x4*)(xin32 + EO_OFF(it) + 4)); }
; #pragma unroll
;             for (int it = 0; it < 16; ++it) {
;                 const int ai = it >> 3, m = (it >> 1) & 3, bj = it & 1;
;                 const f32x4 x0 = xq[it % PF][0], x1 = xq[it % PF][1];
;                 if (it + PF < 16) { xq[it % PF][0] = __builtin_nontemporal_load((const f32x4*)(xin32 + EO_OFF(it + PF))); xq[it % PF][1] = __builtin_nontemporal_load((const f32x4*)(xin32 + EO_OFF(it + PF) + 4)); }
;                 const f32x4 v0 = x0 + gv[bj][0] * acc[ai][bj][m][0], v1 = x1 + gv[bj][1] * acc[ai][bj][m][1];
;                 u32x4 w; w.x = pg8::cvt_pk_bf16(v0[0], v0[1]); w.y = pg8::cvt_pk_bf16(v0[2], v0[3]); w.z = pg8::cvt_pk_bf16(v1[0], v1[1]); w.w = pg8::cvt_pk_bf16(v1[2], v1[3]);
;                 *(u32x4*)(out + EO_OFF(it)) = w;
;             }
.LBB0_720:
	s_ashr_i32 s15, s43, 31
	s_lshr_b32 s15, s15, 28
	s_add_i32 s15, s43, s15
	s_ashr_i32 s15, s15, 4
	s_mul_hi_i32 s17, s15, 0x6000
	s_mulk_i32 s15, 0x6000
	v_lshl_or_b32 v204, s44, 8, v248
	s_add_u32 s22, s36, s15
	s_addc_u32 s23, s37, s17
	v_lshlrev_b32_e32 v205, 2, v204
	s_lshl_b32 s15, s43, 19
	global_load_dwordx4 v[60:63], v205, s[22:23] offset:16
	global_load_dwordx4 v[64:67], v205, s[22:23]
	global_load_dwordx4 v[52:55], v205, s[22:23] offset:528
	global_load_dwordx4 v[56:59], v205, s[22:23] offset:512
	s_add_u32 s26, s50, s15
	s_addc_u32 s27, s51, 0
	v_lshlrev_b32_e32 v207, 1, v204
	v_lshl_add_u32 v206, v1, 12, v205
	v_lshl_add_u32 v207, v1, 11, v207
	s_andn2_b64 vcc, exec, s[12:13]
	s_cbranch_vccnz .Lop_epi_bf16
	s_lshl_b32 s15, s43, 20
	s_add_u32 s24, s8, s15
	s_addc_u32 s25, s9, 0
	s_add_u32 s28, s24, 0x0
	s_addc_u32 s29, s25, 0
	global_load_dwordx4 v[148:151], v206, s[28:29]
	global_load_dwordx4 v[152:155], v206, s[28:29] offset:16
	global_load_dwordx4 v[156:159], v206, s[28:29] offset:512
	global_load_dwordx4 v[160:163], v206, s[28:29] offset:528
	s_add_u32 s28, s24, 0x10000
	s_addc_u32 s29, s25, 0
	global_load_dwordx4 v[164:167], v206, s[28:29]
	global_load_dwordx4 v[168:171], v206, s[28:29] offset:16
	global_load_dwordx4 v[172:175], v206, s[28:29] offset:512
	global_load_dwordx4 v[176:179], v206, s[28:29] offset:528
	s_add_u32 s28, s24, 0x20000
	s_addc_u32 s29, s25, 0
	global_load_dwordx4 v[180:183], v206, s[28:29]
	global_load_dwordx4 v[184:187], v206, s[28:29] offset:16
	global_load_dwordx4 v[208:211], v206, s[28:29] offset:512
	global_load_dwordx4 v[212:215], v206, s[28:29] offset:528
	s_add_u32 s28, s24, 0x30000
	s_addc_u32 s29, s25, 0
	global_load_dwordx4 v[216:219], v206, s[28:29]
	global_load_dwordx4 v[220:223], v206, s[28:29] offset:16
	global_load_dwordx4 v[224:227], v206, s[28:29] offset:512
	global_load_dwordx4 v[228:231], v206, s[28:29] offset:528
	s_add_u32 s32, s26, 0x0
	s_addc_u32 s33, s27, 0
	s_add_u32 s28, s24, 0x80000
	s_addc_u32 s29, s25, 0
	s_waitcnt vmcnt(14)
	v_pk_fma_f32 v[148:149], v[144:145], v[64:65], v[148:149]
	v_pk_fma_f32 v[150:151], v[146:147], v[66:67], v[150:151]
	v_pk_fma_f32 v[152:153], v[140:141], v[60:61], v[152:153]
	v_pk_fma_f32 v[154:155], v[142:143], v[62:63], v[154:155]
	v_cvt_pk_bf16_f32 v148, v148, v149
	v_cvt_pk_bf16_f32 v149, v150, v151
	v_cvt_pk_bf16_f32 v150, v152, v153
	v_cvt_pk_bf16_f32 v151, v154, v155
	global_store_dwordx4 v207, v[148:151], s[32:33] nt
	global_load_dwordx4 v[148:151], v206, s[28:29]
	global_load_dwordx4 v[152:155], v206, s[28:29] offset:16
	s_waitcnt vmcnt(15)
	v_pk_fma_f32 v[156:157], v[136:137], v[56:57], v[156:157]
	v_pk_fma_f32 v[158:159], v[138:139], v[58:59], v[158:159]
	v_pk_fma_f32 v[160:161], v[132:133], v[52:53], v[160:161]
	v_pk_fma_f32 v[162:163], v[134:135], v[54:55], v[162:163]
	v_cvt_pk_bf16_f32 v156, v156, v157
	v_cvt_pk_bf16_f32 v157, v158, v159
	v_cvt_pk_bf16_f32 v158, v160, v161
	v_cvt_pk_bf16_f32 v159, v162, v163
	global_store_dwordx4 v207, v[156:159], s[32:33] offset:256 nt
	global_load_dwordx4 v[156:159], v206, s[28:29] offset:512
	global_load_dwordx4 v[160:163], v206, s[28:29] offset:528
	s_add_u32 s32, s26, 0x8000
	s_addc_u32 s33, s27, 0
	s_add_u32 s28, s24, 0x90000
	s_addc_u32 s29, s25, 0
	s_waitcnt vmcnt(16)
	v_pk_fma_f32 v[164:165], v[128:129], v[64:65], v[164:165]
	v_pk_fma_f32 v[166:167], v[130:131], v[66:67], v[166:167]
	v_pk_fma_f32 v[168:169], v[124:125], v[60:61], v[168:169]
	v_pk_fma_f32 v[170:171], v[126:127], v[62:63], v[170:171]
	v_cvt_pk_bf16_f32 v164, v164, v165
	v_cvt_pk_bf16_f32 v165, v166, v167
	v_cvt_pk_bf16_f32 v166, v168, v169
	v_cvt_pk_bf16_f32 v167, v170, v171
	global_store_dwordx4 v207, v[164:167], s[32:33] nt
	global_load_dwordx4 v[164:167], v206, s[28:29]
	global_load_dwordx4 v[168:171], v206, s[28:29] offset:16
	s_waitcnt vmcnt(17)
	v_pk_fma_f32 v[172:173], v[120:121], v[56:57], v[172:173]
	v_pk_fma_f32 v[174:175], v[122:123], v[58:59], v[174:175]
	v_pk_fma_f32 v[176:177], v[116:117], v[52:53], v[176:177]
	v_pk_fma_f32 v[178:179], v[118:119], v[54:55], v[178:179]
	v_cvt_pk_bf16_f32 v172, v172, v173
	v_cvt_pk_bf16_f32 v173, v174, v175
	v_cvt_pk_bf16_f32 v174, v176, v177
	v_cvt_pk_bf16_f32 v175, v178, v179
	global_store_dwordx4 v207, v[172:175], s[32:33] offset:256 nt
	global_load_dwordx4 v[172:175], v206, s[28:29] offset:512
	global_load_dwordx4 v[176:179], v206, s[28:29] offset:528
	s_add_u32 s32, s26, 0x10000
	s_addc_u32 s33, s27, 0
	s_add_u32 s28, s24, 0xa0000
	s_addc_u32 s29, s25, 0
	s_waitcnt vmcnt(18)
	v_pk_fma_f32 v[180:181], v[112:113], v[64:65], v[180:181]
	v_pk_fma_f32 v[182:183], v[114:115], v[66:67], v[182:183]
	v_pk_fma_f32 v[184:185], v[108:109], v[60:61], v[184:185]
	v_pk_fma_f32 v[186:187], v[110:111], v[62:63], v[186:187]
	v_cvt_pk_bf16_f32 v180, v180, v181
	v_cvt_pk_bf16_f32 v181, v182, v183
	v_cvt_pk_bf16_f32 v182, v184, v185
	v_cvt_pk_bf16_f32 v183, v186, v187
	global_store_dwordx4 v207, v[180:183], s[32:33] nt
	global_load_dwordx4 v[180:183], v206, s[28:29]
	global_load_dwordx4 v[184:187], v206, s[28:29] offset:16
	s_waitcnt vmcnt(19)
	v_pk_fma_f32 v[208:209], v[104:105], v[56:57], v[208:209]
	v_pk_fma_f32 v[210:211], v[106:107], v[58:59], v[210:211]
	v_pk_fma_f32 v[212:213], v[100:101], v[52:53], v[212:213]
	v_pk_fma_f32 v[214:215], v[102:103], v[54:55], v[214:215]
	v_cvt_pk_bf16_f32 v208, v208, v209
	v_cvt_pk_bf16_f32 v209, v210, v211
	v_cvt_pk_bf16_f32 v210, v212, v213
	v_cvt_pk_bf16_f32 v211, v214, v215
	global_store_dwordx4 v207, v[208:211], s[32:33] offset:256 nt
	global_load_dwordx4 v[208:211], v206, s[28:29] offset:512
	global_load_dwordx4 v[212:215], v206, s[28:29] offset:528
	s_add_u32 s32, s26, 0x18000
	s_addc_u32 s33, s27, 0
	s_add_u32 s28, s24, 0xb0000
	s_addc_u32 s29, s25, 0
	s_waitcnt vmcnt(20)
; __device__ __forceinline__ unsigned cvt_pk_bf16(float lo, float hi) { unsigned r; asm volatile("v_cvt_pk_bf16_f32 %0, %1, %2" : "=v"(r) : "v"(lo), "v"(hi)); return r; }
;     __device__ __forceinline__ void operator()(const f32x4 (&acc)[2][2][4][2], const pg8::Unit& u, int wr, int wc, int fr, int fq) const {
;     ...
;             for (int it = 0; it < 16; ++it) {
;                 const int ai = it >> 3, m = (it >> 1) & 3, bj = it & 1;
;                 const f32x4 x0 = xq[it % PF][0], x1 = xq[it % PF][1];
;                 if (it + PF < 16) { xq[it % PF][0] = __builtin_nontemporal_load((const f32x4*)(xin32 + EO_OFF(it + PF))); xq[it % PF][1] = __builtin_nontemporal_load((const f32x4*)(xin32 + EO_OFF(it + PF) + 4)); }
;                 const f32x4 v0 = x0 + gv[bj][0] * acc[ai][bj][m][0], v1 = x1 + gv[bj][1] * acc[ai][bj][m][1];
;                 u32x4 w; w.x = pg8::cvt_pk_bf16(v0[0], v0[1]); w.y = pg8::cvt_pk_bf16(v0[2], v0[3]); w.z = pg8::cvt_pk_bf16(v1[0], v1[1]); w.w = pg8::cvt_pk_bf16(v1[2], v1[3]);
;                 *(u32x4*)(out + EO_OFF(it)) = w;
;             }
	v_pk_fma_f32 v[216:217], v[96:97], v[64:65], v[216:217]
	v_pk_fma_f32 v[218:219], v[98:99], v[66:67], v[218:219]
	v_pk_fma_f32 v[220:221], v[92:93], v[60:61], v[220:221]
	v_pk_fma_f32 v[222:223], v[94:95], v[62:63], v[222:223]
	v_cvt_pk_bf16_f32 v216, v216, v217
	v_cvt_pk_bf16_f32 v217, v218, v219
	v_cvt_pk_bf16_f32 v218, v220, v221
	v_cvt_pk_bf16_f32 v219, v222, v223
	global_store_dwordx4 v207, v[216:219], s[32:33] nt
	global_load_dwordx4 v[216:219], v206, s[28:29]
	global_load_dwordx4 v[220:223], v206, s[28:29] offset:16
	s_waitcnt vmcnt(21)
	v_pk_fma_f32 v[224:225], v[88:89], v[56:57], v[224:225]
	v_pk_fma_f32 v[226:227], v[90:91], v[58:59], v[226:227]
	v_pk_fma_f32 v[228:229], v[84:85], v[52:53], v[228:229]
	v_pk_fma_f32 v[230:231], v[86:87], v[54:55], v[230:231]
	v_cvt_pk_bf16_f32 v224, v224, v225
	v_cvt_pk_bf16_f32 v225, v226, v227
	v_cvt_pk_bf16_f32 v226, v228, v229
	v_cvt_pk_bf16_f32 v227, v230, v231
	global_store_dwordx4 v207, v[224:227], s[32:33] offset:256 nt
	global_load_dwordx4 v[224:227], v206, s[28:29] offset:512
	global_load_dwordx4 v[228:231], v206, s[28:29] offset:528
	s_add_u32 s32, s26, 0x40000
	s_addc_u32 s33, s27, 0
	s_waitcnt vmcnt(21)
	v_pk_fma_f32 v[148:149], v[80:81], v[64:65], v[148:149]
	v_pk_fma_f32 v[150:151], v[82:83], v[66:67], v[150:151]
	v_pk_fma_f32 v[152:153], v[76:77], v[60:61], v[152:153]
	v_pk_fma_f32 v[154:155], v[78:79], v[62:63], v[154:155]
	v_cvt_pk_bf16_f32 v148, v148, v149
	v_cvt_pk_bf16_f32 v149, v150, v151
	v_cvt_pk_bf16_f32 v150, v152, v153
	v_cvt_pk_bf16_f32 v151, v154, v155
	global_store_dwordx4 v207, v[148:151], s[32:33] nt
	s_waitcnt vmcnt(19)
	v_pk_fma_f32 v[156:157], v[72:73], v[56:57], v[156:157]
	v_pk_fma_f32 v[158:159], v[74:75], v[58:59], v[158:159]
	v_pk_fma_f32 v[160:161], v[68:69], v[52:53], v[160:161]
	v_pk_fma_f32 v[162:163], v[70:71], v[54:55], v[162:163]
	v_cvt_pk_bf16_f32 v156, v156, v157
	v_cvt_pk_bf16_f32 v157, v158, v159
	v_cvt_pk_bf16_f32 v158, v160, v161
	v_cvt_pk_bf16_f32 v159, v162, v163
	global_store_dwordx4 v207, v[156:159], s[32:33] offset:256 nt
	s_add_u32 s32, s26, 0x48000
	s_addc_u32 s33, s27, 0
	s_waitcnt vmcnt(17)
	v_pk_fma_f32 v[164:165], v[48:49], v[64:65], v[164:165]
	v_pk_fma_f32 v[166:167], v[50:51], v[66:67], v[166:167]
	v_pk_fma_f32 v[168:169], v[44:45], v[60:61], v[168:169]
	v_pk_fma_f32 v[170:171], v[46:47], v[62:63], v[170:171]
	v_cvt_pk_bf16_f32 v164, v164, v165
	v_cvt_pk_bf16_f32 v165, v166, v167
	v_cvt_pk_bf16_f32 v166, v168, v169
	v_cvt_pk_bf16_f32 v167, v170, v171
	global_store_dwordx4 v207, v[164:167], s[32:33] nt
	s_waitcnt vmcnt(15)
	v_pk_fma_f32 v[172:173], v[40:41], v[56:57], v[172:173]
	v_pk_fma_f32 v[174:175], v[42:43], v[58:59], v[174:175]
	v_pk_fma_f32 v[176:177], v[36:37], v[52:53], v[176:177]
	v_pk_fma_f32 v[178:179], v[38:39], v[54:55], v[178:179]
	v_cvt_pk_bf16_f32 v172, v172, v173
	v_cvt_pk_bf16_f32 v173, v174, v175
	v_cvt_pk_bf16_f32 v174, v176, v177
	v_cvt_pk_bf16_f32 v175, v178, v179
	global_store_dwordx4 v207, v[172:175], s[32:33] offset:256 nt
	s_add_u32 s32, s26, 0x50000
	s_addc_u32 s33, s27, 0
	s_waitcnt vmcnt(13)
	v_pk_fma_f32 v[180:181], v[30:31], v[64:65], v[180:181]
	v_pk_fma_f32 v[182:183], v[32:33], v[66:67], v[182:183]
	v_pk_fma_f32 v[184:185], v[26:27], v[60:61], v[184:185]
	v_pk_fma_f32 v[186:187], v[28:29], v[62:63], v[186:187]
	v_cvt_pk_bf16_f32 v180, v180, v181
	v_cvt_pk_bf16_f32 v181, v182, v183
	v_cvt_pk_bf16_f32 v182, v184, v185
	v_cvt_pk_bf16_f32 v183, v186, v187
	global_store_dwordx4 v207, v[180:183], s[32:33] nt
	s_waitcnt vmcnt(11)
	v_pk_fma_f32 v[208:209], v[22:23], v[56:57], v[208:209]
	v_pk_fma_f32 v[210:211], v[24:25], v[58:59], v[210:211]
	v_pk_fma_f32 v[212:213], v[18:19], v[52:53], v[212:213]
	v_pk_fma_f32 v[214:215], v[20:21], v[54:55], v[214:215]
	v_cvt_pk_bf16_f32 v208, v208, v209
	v_cvt_pk_bf16_f32 v209, v210, v211
	v_cvt_pk_bf16_f32 v210, v212, v213
	v_cvt_pk_bf16_f32 v211, v214, v215
	global_store_dwordx4 v207, v[208:211], s[32:33] offset:256 nt
	s_add_u32 s32, s26, 0x58000
	s_addc_u32 s33, s27, 0
	s_waitcnt vmcnt(9)
	v_pk_fma_f32 v[216:217], v[14:15], v[64:65], v[216:217]
	v_pk_fma_f32 v[218:219], v[16:17], v[66:67], v[218:219]
	v_pk_fma_f32 v[220:221], v[10:11], v[60:61], v[220:221]
	v_pk_fma_f32 v[222:223], v[12:13], v[62:63], v[222:223]
	v_cvt_pk_bf16_f32 v216, v216, v217
	v_cvt_pk_bf16_f32 v217, v218, v219
	v_cvt_pk_bf16_f32 v218, v220, v221
	v_cvt_pk_bf16_f32 v219, v222, v223
	global_store_dwordx4 v207, v[216:219], s[32:33] nt
	s_waitcnt vmcnt(7)
	v_pk_fma_f32 v[224:225], v[6:7], v[56:57], v[224:225]
	v_pk_fma_f32 v[226:227], v[8:9], v[58:59], v[226:227]
	v_pk_fma_f32 v[228:229], v[2:3], v[52:53], v[228:229]
	v_pk_fma_f32 v[230:231], v[4:5], v[54:55], v[230:231]
	v_cvt_pk_bf16_f32 v224, v224, v225
	v_cvt_pk_bf16_f32 v225, v226, v227
	v_cvt_pk_bf16_f32 v226, v228, v229
	v_cvt_pk_bf16_f32 v227, v230, v231
	global_store_dwordx4 v207, v[224:227], s[32:33] offset:256 nt
	s_branch .Lop_epi_done
; __device__ __forceinline__ unsigned cvt_pk_bf16(float lo, float hi) { unsigned r; asm volatile("v_cvt_pk_bf16_f32 %0, %1, %2" : "=v"(r) : "v"(lo), "v"(hi)); return r; }
;     __device__ __forceinline__ void operator()(const f32x4 (&acc)[2][2][4][2], const pg8::Unit& u, int wr, int wc, int fr, int fq) const {
;     ...
;             u32x4 xq[PF];
; #pragma unroll
;             for (int it = 0; it < PF; ++it) xq[it] = __builtin_nontemporal_load((const u32x4*)(xin16 + EO_OFF(it)));
; #pragma unroll
;             for (int it = 0; it < 16; ++it) {
;                 const int ai = it >> 3, m = (it >> 1) & 3, bj = it & 1;
;                 const u32x4 xv = xq[it % PF];
;                 if (it + PF < 16) xq[it % PF] = __builtin_nontemporal_load((const u32x4*)(xin16 + EO_OFF(it + PF)));
;                 const f32x4 x0 = (f32x4){__uint_as_float(xv.x << 16), __uint_as_float(xv.x & 0xffff0000u), __uint_as_float(xv.y << 16), __uint_as_float(xv.y & 0xffff0000u)};
;                 const f32x4 x1 = (f32x4){__uint_as_float(xv.z << 16), __uint_as_float(xv.z & 0xffff0000u), __uint_as_float(xv.w << 16), __uint_as_float(xv.w & 0xffff0000u)};
;                 const f32x4 v0 = x0 + gv[bj][0] * acc[ai][bj][m][0], v1 = x1 + gv[bj][1] * acc[ai][bj][m][1];
;                 u32x4 w; w.x = pg8::cvt_pk_bf16(v0[0], v0[1]); w.y = pg8::cvt_pk_bf16(v0[2], v0[3]); w.z = pg8::cvt_pk_bf16(v1[0], v1[1]); w.w = pg8::cvt_pk_bf16(v1[2], v1[3]);
;                 *(u32x4*)(out + EO_OFF(it)) = w;
;             }
.Lop_epi_bf16:
	s_add_u32 s28, s26, 0x0
	s_addc_u32 s29, s27, 0
	global_load_dwordx4 v[148:151], v207, s[28:29]
	global_load_dwordx4 v[152:155], v207, s[28:29] offset:256
	s_add_u32 s28, s26, 0x8000
	s_addc_u32 s29, s27, 0
	global_load_dwordx4 v[156:159], v207, s[28:29]
	global_load_dwordx4 v[160:163], v207, s[28:29] offset:256
	s_add_u32 s28, s26, 0x10000
	s_addc_u32 s29, s27, 0
	global_load_dwordx4 v[164:167], v207, s[28:29]
	global_load_dwordx4 v[168:171], v207, s[28:29] offset:256
	s_add_u32 s28, s26, 0x18000
	s_addc_u32 s29, s27, 0
	global_load_dwordx4 v[172:175], v207, s[28:29]
	global_load_dwordx4 v[176:179], v207, s[28:29] offset:256
	s_add_u32 s28, s26, 0x40000
	s_addc_u32 s29, s27, 0
	global_load_dwordx4 v[180:183], v207, s[28:29]
	global_load_dwordx4 v[184:187], v207, s[28:29] offset:256
	s_add_u32 s28, s26, 0x48000
	s_addc_u32 s29, s27, 0
	global_load_dwordx4 v[208:211], v207, s[28:29]
	global_load_dwordx4 v[212:215], v207, s[28:29] offset:256
	s_add_u32 s28, s26, 0x50000
	s_addc_u32 s29, s27, 0
	global_load_dwordx4 v[216:219], v207, s[28:29]
	global_load_dwordx4 v[220:223], v207, s[28:29] offset:256
	s_add_u32 s28, s26, 0x58000
	s_addc_u32 s29, s27, 0
	global_load_dwordx4 v[224:227], v207, s[28:29]
	global_load_dwordx4 v[228:231], v207, s[28:29] offset:256
	s_add_u32 s32, s26, 0x0
	s_addc_u32 s33, s27, 0
	s_waitcnt vmcnt(15)
	v_lshlrev_b32_e32 v232, 16, v148
	v_and_b32_e32 v233, 0xffff0000, v148
	v_lshlrev_b32_e32 v234, 16, v149
	v_and_b32_e32 v235, 0xffff0000, v149
	v_lshlrev_b32_e32 v244, 16, v150
	v_and_b32_e32 v245, 0xffff0000, v150
	v_lshlrev_b32_e32 v246, 16, v151
	v_and_b32_e32 v247, 0xffff0000, v151
	v_pk_fma_f32 v[144:145], v[144:145], v[64:65], v[232:233]
	v_pk_fma_f32 v[146:147], v[146:147], v[66:67], v[234:235]
	v_pk_fma_f32 v[140:141], v[140:141], v[60:61], v[244:245]
	v_pk_fma_f32 v[142:143], v[142:143], v[62:63], v[246:247]
	v_cvt_pk_bf16_f32 v148, v144, v145
	v_cvt_pk_bf16_f32 v149, v146, v147
	v_cvt_pk_bf16_f32 v150, v140, v141
	v_cvt_pk_bf16_f32 v151, v142, v143
	global_store_dwordx4 v207, v[148:151], s[32:33] nt
	s_waitcnt vmcnt(15)
	v_lshlrev_b32_e32 v232, 16, v152
	v_and_b32_e32 v233, 0xffff0000, v152
	v_lshlrev_b32_e32 v234, 16, v153
	v_and_b32_e32 v235, 0xffff0000, v153
	v_lshlrev_b32_e32 v244, 16, v154
	v_and_b32_e32 v245, 0xffff0000, v154
	v_lshlrev_b32_e32 v246, 16, v155
	v_and_b32_e32 v247, 0xffff0000, v155
	v_pk_fma_f32 v[136:137], v[136:137], v[56:57], v[232:233]
	v_pk_fma_f32 v[138:139], v[138:139], v[58:59], v[234:235]
	v_pk_fma_f32 v[132:133], v[132:133], v[52:53], v[244:245]
	v_pk_fma_f32 v[134:135], v[134:135], v[54:55], v[246:247]
	v_cvt_pk_bf16_f32 v152, v136, v137
	v_cvt_pk_bf16_f32 v153, v138, v139
	v_cvt_pk_bf16_f32 v154, v132, v133
	v_cvt_pk_bf16_f32 v155, v134, v135
	global_store_dwordx4 v207, v[152:155], s[32:33] offset:256 nt
	s_add_u32 s32, s26, 0x8000
	s_addc_u32 s33, s27, 0
	s_waitcnt vmcnt(15)
	v_lshlrev_b32_e32 v232, 16, v156
	v_and_b32_e32 v233, 0xffff0000, v156
	v_lshlrev_b32_e32 v234, 16, v157
	v_and_b32_e32 v235, 0xffff0000, v157
	v_lshlrev_b32_e32 v244, 16, v158
	v_and_b32_e32 v245, 0xffff0000, v158
	v_lshlrev_b32_e32 v246, 16, v159
	v_and_b32_e32 v247, 0xffff0000, v159
	v_pk_fma_f32 v[128:129], v[128:129], v[64:65], v[232:233]
	v_pk_fma_f32 v[130:131], v[130:131], v[66:67], v[234:235]
	v_pk_fma_f32 v[124:125], v[124:125], v[60:61], v[244:245]
	v_pk_fma_f32 v[126:127], v[126:127], v[62:63], v[246:247]
	v_cvt_pk_bf16_f32 v156, v128, v129
	v_cvt_pk_bf16_f32 v157, v130, v131
	v_cvt_pk_bf16_f32 v158, v124, v125
	v_cvt_pk_bf16_f32 v159, v126, v127
	global_store_dwordx4 v207, v[156:159], s[32:33] nt
	s_waitcnt vmcnt(15)
	v_lshlrev_b32_e32 v232, 16, v160
	v_and_b32_e32 v233, 0xffff0000, v160
	v_lshlrev_b32_e32 v234, 16, v161
	v_and_b32_e32 v235, 0xffff0000, v161
	v_lshlrev_b32_e32 v244, 16, v162
	v_and_b32_e32 v245, 0xffff0000, v162
	v_lshlrev_b32_e32 v246, 16, v163
	v_and_b32_e32 v247, 0xffff0000, v163
	v_pk_fma_f32 v[120:121], v[120:121], v[56:57], v[232:233]
	v_pk_fma_f32 v[122:123], v[122:123], v[58:59], v[234:235]
	v_pk_fma_f32 v[116:117], v[116:117], v[52:53], v[244:245]
	v_pk_fma_f32 v[118:119], v[118:119], v[54:55], v[246:247]
	v_cvt_pk_bf16_f32 v160, v120, v121
	v_cvt_pk_bf16_f32 v161, v122, v123
	v_cvt_pk_bf16_f32 v162, v116, v117
	v_cvt_pk_bf16_f32 v163, v118, v119
	global_store_dwordx4 v207, v[160:163], s[32:33] offset:256 nt
	s_add_u32 s32, s26, 0x10000
	s_addc_u32 s33, s27, 0
	s_waitcnt vmcnt(15)
	v_lshlrev_b32_e32 v232, 16, v164
	v_and_b32_e32 v233, 0xffff0000, v164
	v_lshlrev_b32_e32 v234, 16, v165
	v_and_b32_e32 v235, 0xffff0000, v165
	v_lshlrev_b32_e32 v244, 16, v166
	v_and_b32_e32 v245, 0xffff0000, v166
	v_lshlrev_b32_e32 v246, 16, v167
	v_and_b32_e32 v247, 0xffff0000, v167
	v_pk_fma_f32 v[112:113], v[112:113], v[64:65], v[232:233]
	v_pk_fma_f32 v[114:115], v[114:115], v[66:67], v[234:235]
	v_pk_fma_f32 v[108:109], v[108:109], v[60:61], v[244:245]
	v_pk_fma_f32 v[110:111], v[110:111], v[62:63], v[246:247]
	v_cvt_pk_bf16_f32 v164, v112, v113
	v_cvt_pk_bf16_f32 v165, v114, v115
	v_cvt_pk_bf16_f32 v166, v108, v109
	v_cvt_pk_bf16_f32 v167, v110, v111
	global_store_dwordx4 v207, v[164:167], s[32:33] nt
	s_waitcnt vmcnt(15)
	v_lshlrev_b32_e32 v232, 16, v168
	v_and_b32_e32 v233, 0xffff0000, v168
	v_lshlrev_b32_e32 v234, 16, v169
	v_and_b32_e32 v235, 0xffff0000, v169
	v_lshlrev_b32_e32 v244, 16, v170
	v_and_b32_e32 v245, 0xffff0000, v170
	v_lshlrev_b32_e32 v246, 16, v171
	v_and_b32_e32 v247, 0xffff0000, v171
	v_pk_fma_f32 v[104:105], v[104:105], v[56:57], v[232:233]
	v_pk_fma_f32 v[106:107], v[106:107], v[58:59], v[234:235]
	v_pk_fma_f32 v[100:101], v[100:101], v[52:53], v[244:245]
	v_pk_fma_f32 v[102:103], v[102:103], v[54:55], v[246:247]
	v_cvt_pk_bf16_f32 v168, v104, v105
	v_cvt_pk_bf16_f32 v169, v106, v107
	v_cvt_pk_bf16_f32 v170, v100, v101
	v_cvt_pk_bf16_f32 v171, v102, v103
	global_store_dwordx4 v207, v[168:171], s[32:33] offset:256 nt
	s_add_u32 s32, s26, 0x18000
	s_addc_u32 s33, s27, 0
	s_waitcnt vmcnt(15)
; __device__ __forceinline__ unsigned cvt_pk_bf16(float lo, float hi) { unsigned r; asm volatile("v_cvt_pk_bf16_f32 %0, %1, %2" : "=v"(r) : "v"(lo), "v"(hi)); return r; }
;     __device__ __forceinline__ void operator()(const f32x4 (&acc)[2][2][4][2], const pg8::Unit& u, int wr, int wc, int fr, int fq) const {
;     ...
;             for (int it = 0; it < 16; ++it) {
;                 const int ai = it >> 3, m = (it >> 1) & 3, bj = it & 1;
;                 const u32x4 xv = xq[it % PF];
;                 if (it + PF < 16) xq[it % PF] = __builtin_nontemporal_load((const u32x4*)(xin16 + EO_OFF(it + PF)));
;                 const f32x4 x0 = (f32x4){__uint_as_float(xv.x << 16), __uint_as_float(xv.x & 0xffff0000u), __uint_as_float(xv.y << 16), __uint_as_float(xv.y & 0xffff0000u)};
;                 const f32x4 x1 = (f32x4){__uint_as_float(xv.z << 16), __uint_as_float(xv.z & 0xffff0000u), __uint_as_float(xv.w << 16), __uint_as_float(xv.w & 0xffff0000u)};
;                 const f32x4 v0 = x0 + gv[bj][0] * acc[ai][bj][m][0], v1 = x1 + gv[bj][1] * acc[ai][bj][m][1];
;                 u32x4 w; w.x = pg8::cvt_pk_bf16(v0[0], v0[1]); w.y = pg8::cvt_pk_bf16(v0[2], v0[3]); w.z = pg8::cvt_pk_bf16(v1[0], v1[1]); w.w = pg8::cvt_pk_bf16(v1[2], v1[3]);
;                 *(u32x4*)(out + EO_OFF(it)) = w;
;             }
	v_lshlrev_b32_e32 v232, 16, v172
	v_and_b32_e32 v233, 0xffff0000, v172
	v_lshlrev_b32_e32 v234, 16, v173
	v_and_b32_e32 v235, 0xffff0000, v173
	v_lshlrev_b32_e32 v244, 16, v174
	v_and_b32_e32 v245, 0xffff0000, v174
	v_lshlrev_b32_e32 v246, 16, v175
	v_and_b32_e32 v247, 0xffff0000, v175
	v_pk_fma_f32 v[96:97], v[96:97], v[64:65], v[232:233]
	v_pk_fma_f32 v[98:99], v[98:99], v[66:67], v[234:235]
	v_pk_fma_f32 v[92:93], v[92:93], v[60:61], v[244:245]
	v_pk_fma_f32 v[94:95], v[94:95], v[62:63], v[246:247]
	v_cvt_pk_bf16_f32 v172, v96, v97
	v_cvt_pk_bf16_f32 v173, v98, v99
	v_cvt_pk_bf16_f32 v174, v92, v93
	v_cvt_pk_bf16_f32 v175, v94, v95
	global_store_dwordx4 v207, v[172:175], s[32:33] nt
	s_waitcnt vmcnt(15)
	v_lshlrev_b32_e32 v232, 16, v176
	v_and_b32_e32 v233, 0xffff0000, v176
	v_lshlrev_b32_e32 v234, 16, v177
	v_and_b32_e32 v235, 0xffff0000, v177
	v_lshlrev_b32_e32 v244, 16, v178
	v_and_b32_e32 v245, 0xffff0000, v178
	v_lshlrev_b32_e32 v246, 16, v179
	v_and_b32_e32 v247, 0xffff0000, v179
	v_pk_fma_f32 v[88:89], v[88:89], v[56:57], v[232:233]
	v_pk_fma_f32 v[90:91], v[90:91], v[58:59], v[234:235]
	v_pk_fma_f32 v[84:85], v[84:85], v[52:53], v[244:245]
	v_pk_fma_f32 v[86:87], v[86:87], v[54:55], v[246:247]
	v_cvt_pk_bf16_f32 v176, v88, v89
	v_cvt_pk_bf16_f32 v177, v90, v91
	v_cvt_pk_bf16_f32 v178, v84, v85
	v_cvt_pk_bf16_f32 v179, v86, v87
	global_store_dwordx4 v207, v[176:179], s[32:33] offset:256 nt
	s_add_u32 s32, s26, 0x40000
	s_addc_u32 s33, s27, 0
	s_waitcnt vmcnt(15)
	v_lshlrev_b32_e32 v232, 16, v180
	v_and_b32_e32 v233, 0xffff0000, v180
	v_lshlrev_b32_e32 v234, 16, v181
	v_and_b32_e32 v235, 0xffff0000, v181
	v_lshlrev_b32_e32 v244, 16, v182
	v_and_b32_e32 v245, 0xffff0000, v182
	v_lshlrev_b32_e32 v246, 16, v183
	v_and_b32_e32 v247, 0xffff0000, v183
	v_pk_fma_f32 v[80:81], v[80:81], v[64:65], v[232:233]
	v_pk_fma_f32 v[82:83], v[82:83], v[66:67], v[234:235]
	v_pk_fma_f32 v[76:77], v[76:77], v[60:61], v[244:245]
	v_pk_fma_f32 v[78:79], v[78:79], v[62:63], v[246:247]
	v_cvt_pk_bf16_f32 v180, v80, v81
	v_cvt_pk_bf16_f32 v181, v82, v83
	v_cvt_pk_bf16_f32 v182, v76, v77
	v_cvt_pk_bf16_f32 v183, v78, v79
	global_store_dwordx4 v207, v[180:183], s[32:33] nt
	s_waitcnt vmcnt(15)
	v_lshlrev_b32_e32 v232, 16, v184
	v_and_b32_e32 v233, 0xffff0000, v184
	v_lshlrev_b32_e32 v234, 16, v185
	v_and_b32_e32 v235, 0xffff0000, v185
	v_lshlrev_b32_e32 v244, 16, v186
	v_and_b32_e32 v245, 0xffff0000, v186
	v_lshlrev_b32_e32 v246, 16, v187
	v_and_b32_e32 v247, 0xffff0000, v187
	v_pk_fma_f32 v[72:73], v[72:73], v[56:57], v[232:233]
	v_pk_fma_f32 v[74:75], v[74:75], v[58:59], v[234:235]
	v_pk_fma_f32 v[68:69], v[68:69], v[52:53], v[244:245]
	v_pk_fma_f32 v[70:71], v[70:71], v[54:55], v[246:247]
	v_cvt_pk_bf16_f32 v184, v72, v73
	v_cvt_pk_bf16_f32 v185, v74, v75
	v_cvt_pk_bf16_f32 v186, v68, v69
	v_cvt_pk_bf16_f32 v187, v70, v71
	global_store_dwordx4 v207, v[184:187], s[32:33] offset:256 nt
	s_add_u32 s32, s26, 0x48000
	s_addc_u32 s33, s27, 0
	s_waitcnt vmcnt(15)
	v_lshlrev_b32_e32 v232, 16, v208
	v_and_b32_e32 v233, 0xffff0000, v208
	v_lshlrev_b32_e32 v234, 16, v209
	v_and_b32_e32 v235, 0xffff0000, v209
	v_lshlrev_b32_e32 v244, 16, v210
	v_and_b32_e32 v245, 0xffff0000, v210
	v_lshlrev_b32_e32 v246, 16, v211
	v_and_b32_e32 v247, 0xffff0000, v211
	v_pk_fma_f32 v[48:49], v[48:49], v[64:65], v[232:233]
	v_pk_fma_f32 v[50:51], v[50:51], v[66:67], v[234:235]
	v_pk_fma_f32 v[44:45], v[44:45], v[60:61], v[244:245]
	v_pk_fma_f32 v[46:47], v[46:47], v[62:63], v[246:247]
	v_cvt_pk_bf16_f32 v208, v48, v49
	v_cvt_pk_bf16_f32 v209, v50, v51
	v_cvt_pk_bf16_f32 v210, v44, v45
	v_cvt_pk_bf16_f32 v211, v46, v47
	global_store_dwordx4 v207, v[208:211], s[32:33] nt
	s_waitcnt vmcnt(15)
; __device__ __forceinline__ unsigned cvt_pk_bf16(float lo, float hi) { unsigned r; asm volatile("v_cvt_pk_bf16_f32 %0, %1, %2" : "=v"(r) : "v"(lo), "v"(hi)); return r; }
;     __device__ __forceinline__ void operator()(const f32x4 (&acc)[2][2][4][2], const pg8::Unit& u, int wr, int wc, int fr, int fq) const {
;     ...
;             for (int it = 0; it < 16; ++it) {
;                 const int ai = it >> 3, m = (it >> 1) & 3, bj = it & 1;
;                 const u32x4 xv = xq[it % PF];
;                 if (it + PF < 16) xq[it % PF] = __builtin_nontemporal_load((const u32x4*)(xin16 + EO_OFF(it + PF)));
;                 const f32x4 x0 = (f32x4){__uint_as_float(xv.x << 16), __uint_as_float(xv.x & 0xffff0000u), __uint_as_float(xv.y << 16), __uint_as_float(xv.y & 0xffff0000u)};
;                 const f32x4 x1 = (f32x4){__uint_as_float(xv.z << 16), __uint_as_float(xv.z & 0xffff0000u), __uint_as_float(xv.w << 16), __uint_as_float(xv.w & 0xffff0000u)};
;                 const f32x4 v0 = x0 + gv[bj][0] * acc[ai][bj][m][0], v1 = x1 + gv[bj][1] * acc[ai][bj][m][1];
;                 u32x4 w; w.x = pg8::cvt_pk_bf16(v0[0], v0[1]); w.y = pg8::cvt_pk_bf16(v0[2], v0[3]); w.z = pg8::cvt_pk_bf16(v1[0], v1[1]); w.w = pg8::cvt_pk_bf16(v1[2], v1[3]);
;                 *(u32x4*)(out + EO_OFF(it)) = w;
;             }
	v_lshlrev_b32_e32 v232, 16, v212
	v_and_b32_e32 v233, 0xffff0000, v212
	v_lshlrev_b32_e32 v234, 16, v213
	v_and_b32_e32 v235, 0xffff0000, v213
	v_lshlrev_b32_e32 v244, 16, v214
	v_and_b32_e32 v245, 0xffff0000, v214
	v_lshlrev_b32_e32 v246, 16, v215
	v_and_b32_e32 v247, 0xffff0000, v215
	v_pk_fma_f32 v[40:41], v[40:41], v[56:57], v[232:233]
	v_pk_fma_f32 v[42:43], v[42:43], v[58:59], v[234:235]
	v_pk_fma_f32 v[36:37], v[36:37], v[52:53], v[244:245]
	v_pk_fma_f32 v[38:39], v[38:39], v[54:55], v[246:247]
	v_cvt_pk_bf16_f32 v212, v40, v41
	v_cvt_pk_bf16_f32 v213, v42, v43
	v_cvt_pk_bf16_f32 v214, v36, v37
	v_cvt_pk_bf16_f32 v215, v38, v39
	global_store_dwordx4 v207, v[212:215], s[32:33] offset:256 nt
	s_add_u32 s32, s26, 0x50000
	s_addc_u32 s33, s27, 0
	s_waitcnt vmcnt(15)
	v_lshlrev_b32_e32 v232, 16, v216
	v_and_b32_e32 v233, 0xffff0000, v216
	v_lshlrev_b32_e32 v234, 16, v217
	v_and_b32_e32 v235, 0xffff0000, v217
	v_lshlrev_b32_e32 v244, 16, v218
	v_and_b32_e32 v245, 0xffff0000, v218
	v_lshlrev_b32_e32 v246, 16, v219
	v_and_b32_e32 v247, 0xffff0000, v219
	v_pk_fma_f32 v[30:31], v[30:31], v[64:65], v[232:233]
	v_pk_fma_f32 v[32:33], v[32:33], v[66:67], v[234:235]
	v_pk_fma_f32 v[26:27], v[26:27], v[60:61], v[244:245]
	v_pk_fma_f32 v[28:29], v[28:29], v[62:63], v[246:247]
	v_cvt_pk_bf16_f32 v216, v30, v31
	v_cvt_pk_bf16_f32 v217, v32, v33
	v_cvt_pk_bf16_f32 v218, v26, v27
	v_cvt_pk_bf16_f32 v219, v28, v29
	global_store_dwordx4 v207, v[216:219], s[32:33] nt
	s_waitcnt vmcnt(15)
	v_lshlrev_b32_e32 v232, 16, v220
	v_and_b32_e32 v233, 0xffff0000, v220
	v_lshlrev_b32_e32 v234, 16, v221
	v_and_b32_e32 v235, 0xffff0000, v221
	v_lshlrev_b32_e32 v244, 16, v222
	v_and_b32_e32 v245, 0xffff0000, v222
	v_lshlrev_b32_e32 v246, 16, v223
	v_and_b32_e32 v247, 0xffff0000, v223
	v_pk_fma_f32 v[22:23], v[22:23], v[56:57], v[232:233]
	v_pk_fma_f32 v[24:25], v[24:25], v[58:59], v[234:235]
	v_pk_fma_f32 v[18:19], v[18:19], v[52:53], v[244:245]
	v_pk_fma_f32 v[20:21], v[20:21], v[54:55], v[246:247]
	v_cvt_pk_bf16_f32 v220, v22, v23
	v_cvt_pk_bf16_f32 v221, v24, v25
	v_cvt_pk_bf16_f32 v222, v18, v19
	v_cvt_pk_bf16_f32 v223, v20, v21
	global_store_dwordx4 v207, v[220:223], s[32:33] offset:256 nt
	s_add_u32 s32, s26, 0x58000
	s_addc_u32 s33, s27, 0
	s_waitcnt vmcnt(15)
	v_lshlrev_b32_e32 v232, 16, v224
	v_and_b32_e32 v233, 0xffff0000, v224
	v_lshlrev_b32_e32 v234, 16, v225
	v_and_b32_e32 v235, 0xffff0000, v225
	v_lshlrev_b32_e32 v244, 16, v226
	v_and_b32_e32 v245, 0xffff0000, v226
	v_lshlrev_b32_e32 v246, 16, v227
	v_and_b32_e32 v247, 0xffff0000, v227
	v_pk_fma_f32 v[14:15], v[14:15], v[64:65], v[232:233]
	v_pk_fma_f32 v[16:17], v[16:17], v[66:67], v[234:235]
	v_pk_fma_f32 v[10:11], v[10:11], v[60:61], v[244:245]
	v_pk_fma_f32 v[12:13], v[12:13], v[62:63], v[246:247]
	v_cvt_pk_bf16_f32 v224, v14, v15
	v_cvt_pk_bf16_f32 v225, v16, v17
	v_cvt_pk_bf16_f32 v226, v10, v11
	v_cvt_pk_bf16_f32 v227, v12, v13
	global_store_dwordx4 v207, v[224:227], s[32:33] nt
	s_waitcnt vmcnt(15)
	v_lshlrev_b32_e32 v232, 16, v228
	v_and_b32_e32 v233, 0xffff0000, v228
	v_lshlrev_b32_e32 v234, 16, v229
	v_and_b32_e32 v235, 0xffff0000, v229
	v_lshlrev_b32_e32 v244, 16, v230
	v_and_b32_e32 v245, 0xffff0000, v230
	v_lshlrev_b32_e32 v246, 16, v231
	v_and_b32_e32 v247, 0xffff0000, v231
	v_pk_fma_f32 v[6:7], v[6:7], v[56:57], v[232:233]
	v_pk_fma_f32 v[8:9], v[8:9], v[58:59], v[234:235]
	v_pk_fma_f32 v[2:3], v[2:3], v[52:53], v[244:245]
	v_pk_fma_f32 v[4:5], v[4:5], v[54:55], v[246:247]
	v_cvt_pk_bf16_f32 v228, v6, v7
	v_cvt_pk_bf16_f32 v229, v8, v9
	v_cvt_pk_bf16_f32 v230, v2, v3
	v_cvt_pk_bf16_f32 v231, v4, v5
	global_store_dwordx4 v207, v[228:231], s[32:33] offset:256 nt
